# attention out-projection epilogue rewritten: all 32 residual loads of a tile issued up front, counted waits (was 16 dependent load-wait-store groups); on top of gating + topk
# baseline (speedup 1.0000x reference)
.Lrs_a_new:
	v_lshlrev_b32_e32 v228, 1, v142
	v_add_u32_e32 v229, 0x4000, v228
	s_mov_b64 s[0:1], s[48:49]
	global_load_dwordx2 v[152:153], v228, s[0:1] nt
	global_load_dwordx2 v[154:155], v228, s[0:1] offset:64 nt
	global_load_dwordx2 v[156:157], v229, s[0:1] nt
	global_load_dwordx2 v[158:159], v229, s[0:1] offset:64 nt
	s_add_u32 s0, s48, 0x8000
	s_addc_u32 s1, s49, 0
	global_load_dwordx2 v[160:161], v228, s[0:1] nt
	global_load_dwordx2 v[162:163], v228, s[0:1] offset:64 nt
	global_load_dwordx2 v[164:165], v229, s[0:1] nt
	global_load_dwordx2 v[166:167], v229, s[0:1] offset:64 nt
	s_add_u32 s0, s48, 0x10000
	s_addc_u32 s1, s49, 0
	global_load_dwordx2 v[168:169], v228, s[0:1] nt
	global_load_dwordx2 v[170:171], v228, s[0:1] offset:64 nt
	global_load_dwordx2 v[172:173], v229, s[0:1] nt
	global_load_dwordx2 v[174:175], v229, s[0:1] offset:64 nt
	s_add_u32 s0, s48, 0x18000
	s_addc_u32 s1, s49, 0
	global_load_dwordx2 v[176:177], v228, s[0:1] nt
	global_load_dwordx2 v[178:179], v228, s[0:1] offset:64 nt
	global_load_dwordx2 v[180:181], v229, s[0:1] nt
	global_load_dwordx2 v[182:183], v229, s[0:1] offset:64 nt
	s_add_u32 s0, s48, 0x40000
	s_addc_u32 s1, s49, 0
	global_load_dwordx2 v[184:185], v228, s[0:1] nt
	global_load_dwordx2 v[186:187], v228, s[0:1] offset:64 nt
	global_load_dwordx2 v[188:189], v229, s[0:1] nt
	global_load_dwordx2 v[190:191], v229, s[0:1] offset:64 nt
	s_add_u32 s0, s48, 0x48000
	s_addc_u32 s1, s49, 0
	global_load_dwordx2 v[192:193], v228, s[0:1] nt
	global_load_dwordx2 v[194:195], v228, s[0:1] offset:64 nt
	global_load_dwordx2 v[196:197], v229, s[0:1] nt
	global_load_dwordx2 v[198:199], v229, s[0:1] offset:64 nt
	s_add_u32 s0, s48, 0x50000
	s_addc_u32 s1, s49, 0
	global_load_dwordx2 v[208:209], v228, s[0:1] nt
	global_load_dwordx2 v[210:211], v228, s[0:1] offset:64 nt
	global_load_dwordx2 v[212:213], v229, s[0:1] nt
	global_load_dwordx2 v[214:215], v229, s[0:1] offset:64 nt
	s_add_u32 s0, s48, 0x58000
	s_addc_u32 s1, s49, 0
	global_load_dwordx2 v[216:217], v228, s[0:1] nt
	global_load_dwordx2 v[218:219], v228, s[0:1] offset:64 nt
	global_load_dwordx2 v[220:221], v229, s[0:1] nt
	global_load_dwordx2 v[222:223], v229, s[0:1] offset:64 nt
	s_mov_b64 s[42:43], s[52:53]
	s_waitcnt vmcnt(28)
	v_lshlrev_b32_e32 v236, 16, v152
	v_and_b32_e32 v237, 0xffff0000, v152
	v_lshlrev_b32_e32 v238, 16, v153
	v_and_b32_e32 v239, 0xffff0000, v153
	v_lshlrev_b32_e32 v240, 16, v156
	v_and_b32_e32 v241, 0xffff0000, v156
	v_lshlrev_b32_e32 v242, 16, v157
	v_and_b32_e32 v243, 0xffff0000, v157
	v_pk_add_f32 v[236:237], v[236:237], v[144:145]
	v_pk_add_f32 v[238:239], v[238:239], v[146:147]
	v_pk_add_f32 v[240:241], v[240:241], v[122:123]
	v_pk_add_f32 v[242:243], v[242:243], v[124:125]
	v_pk_add_f32 v[236:237], v[236:237], 0 op_sel_hi:[1,0]
	v_pk_add_f32 v[238:239], v[238:239], 0 op_sel_hi:[1,0]
	v_pk_add_f32 v[240:241], v[240:241], 0 op_sel_hi:[1,0]
	v_pk_add_f32 v[242:243], v[242:243], 0 op_sel_hi:[1,0]
	s_nop 0
	v_cvt_pk_bf16_f32 v244, v236, v237
	v_cvt_pk_bf16_f32 v245, v238, v239
	v_cvt_pk_bf16_f32 v246, v240, v241
	v_cvt_pk_bf16_f32 v247, v242, v243
	global_store_dwordx2 v228, v[244:245], s[42:43]
	global_store_dwordx2 v229, v[246:247], s[42:43]
	v_mov_b32_e32 v232, v118
	v_mov_b32_e32 v233, v119
	v_mov_b32_e32 v234, v120
	v_mov_b32_e32 v235, v121
	v_mov_b32_dpp v232, v114 row_ror:8 row_mask:0xf bank_mask:0xc
	v_mov_b32_dpp v114, v118 row_ror:8 row_mask:0xf bank_mask:0x3
	v_mov_b32_dpp v233, v115 row_ror:8 row_mask:0xf bank_mask:0xc
	v_mov_b32_dpp v115, v119 row_ror:8 row_mask:0xf bank_mask:0x3
	v_mov_b32_dpp v234, v116 row_ror:8 row_mask:0xf bank_mask:0xc
	v_mov_b32_dpp v116, v120 row_ror:8 row_mask:0xf bank_mask:0x3
	v_mov_b32_dpp v235, v117 row_ror:8 row_mask:0xf bank_mask:0xc
	v_mov_b32_dpp v117, v121 row_ror:8 row_mask:0xf bank_mask:0x3
	v_lshlrev_b32_e32 v236, 16, v154
	v_and_b32_e32 v237, 0xffff0000, v154
	v_lshlrev_b32_e32 v238, 16, v155
	v_and_b32_e32 v239, 0xffff0000, v155
	v_lshlrev_b32_e32 v240, 16, v158
	v_and_b32_e32 v241, 0xffff0000, v158
	v_lshlrev_b32_e32 v242, 16, v159
	v_and_b32_e32 v243, 0xffff0000, v159
	v_pk_add_f32 v[236:237], v[236:237], v[232:233]
	v_pk_add_f32 v[238:239], v[238:239], v[234:235]
	v_pk_add_f32 v[240:241], v[240:241], v[114:115]
	v_pk_add_f32 v[242:243], v[242:243], v[116:117]
	v_pk_add_f32 v[236:237], v[236:237], 0 op_sel_hi:[1,0]
	v_pk_add_f32 v[238:239], v[238:239], 0 op_sel_hi:[1,0]
	v_pk_add_f32 v[240:241], v[240:241], 0 op_sel_hi:[1,0]
	v_pk_add_f32 v[242:243], v[242:243], 0 op_sel_hi:[1,0]
	s_nop 0
	v_cvt_pk_bf16_f32 v130, v236, v237
	v_cvt_pk_bf16_f32 v131, v238, v239
	v_cvt_pk_bf16_f32 v132, v240, v241
	v_cvt_pk_bf16_f32 v133, v242, v243
	global_store_dwordx2 v228, v[130:131], s[42:43] offset:64
	global_store_dwordx2 v229, v[132:133], s[42:43] offset:64
	s_add_u32 s42, s52, 0x8000
	s_addc_u32 s43, s53, 0
	s_waitcnt vmcnt(28)
	v_mov_b32_e32 v232, v110
	v_mov_b32_e32 v233, v111
	v_mov_b32_e32 v234, v112
	v_mov_b32_e32 v235, v113
	v_mov_b32_dpp v232, v106 row_ror:8 row_mask:0xf bank_mask:0xc
	v_mov_b32_dpp v106, v110 row_ror:8 row_mask:0xf bank_mask:0x3
	v_mov_b32_dpp v233, v107 row_ror:8 row_mask:0xf bank_mask:0xc
	v_mov_b32_dpp v107, v111 row_ror:8 row_mask:0xf bank_mask:0x3
	v_mov_b32_dpp v234, v108 row_ror:8 row_mask:0xf bank_mask:0xc
	v_mov_b32_dpp v108, v112 row_ror:8 row_mask:0xf bank_mask:0x3
	v_mov_b32_dpp v235, v109 row_ror:8 row_mask:0xf bank_mask:0xc
	v_mov_b32_dpp v109, v113 row_ror:8 row_mask:0xf bank_mask:0x3
	v_lshlrev_b32_e32 v236, 16, v160
	v_and_b32_e32 v237, 0xffff0000, v160
	v_lshlrev_b32_e32 v238, 16, v161
	v_and_b32_e32 v239, 0xffff0000, v161
	v_lshlrev_b32_e32 v240, 16, v164
	v_and_b32_e32 v241, 0xffff0000, v164
	v_lshlrev_b32_e32 v242, 16, v165
	v_and_b32_e32 v243, 0xffff0000, v165
	v_pk_add_f32 v[236:237], v[236:237], v[232:233]
	v_pk_add_f32 v[238:239], v[238:239], v[234:235]
	v_pk_add_f32 v[240:241], v[240:241], v[106:107]
	v_pk_add_f32 v[242:243], v[242:243], v[108:109]
	v_pk_add_f32 v[236:237], v[236:237], 0 op_sel_hi:[1,0]
	v_pk_add_f32 v[238:239], v[238:239], 0 op_sel_hi:[1,0]
	v_pk_add_f32 v[240:241], v[240:241], 0 op_sel_hi:[1,0]
	v_pk_add_f32 v[242:243], v[242:243], 0 op_sel_hi:[1,0]
	s_nop 0
	v_cvt_pk_bf16_f32 v244, v236, v237
	v_cvt_pk_bf16_f32 v245, v238, v239
	v_cvt_pk_bf16_f32 v246, v240, v241
	v_cvt_pk_bf16_f32 v247, v242, v243
	global_store_dwordx2 v228, v[244:245], s[42:43]
	global_store_dwordx2 v229, v[246:247], s[42:43]
	v_mov_b32_e32 v232, v102
	v_mov_b32_e32 v233, v103
	v_mov_b32_e32 v234, v104
	v_mov_b32_e32 v235, v105
	v_mov_b32_dpp v232, v98 row_ror:8 row_mask:0xf bank_mask:0xc
	v_mov_b32_dpp v98, v102 row_ror:8 row_mask:0xf bank_mask:0x3
	v_mov_b32_dpp v233, v99 row_ror:8 row_mask:0xf bank_mask:0xc
	v_mov_b32_dpp v99, v103 row_ror:8 row_mask:0xf bank_mask:0x3
	v_mov_b32_dpp v234, v100 row_ror:8 row_mask:0xf bank_mask:0xc
	v_mov_b32_dpp v100, v104 row_ror:8 row_mask:0xf bank_mask:0x3
	v_mov_b32_dpp v235, v101 row_ror:8 row_mask:0xf bank_mask:0xc
	v_mov_b32_dpp v101, v105 row_ror:8 row_mask:0xf bank_mask:0x3
	v_lshlrev_b32_e32 v236, 16, v162
	v_and_b32_e32 v237, 0xffff0000, v162
	v_lshlrev_b32_e32 v238, 16, v163
	v_and_b32_e32 v239, 0xffff0000, v163
	v_lshlrev_b32_e32 v240, 16, v166
	v_and_b32_e32 v241, 0xffff0000, v166
	v_lshlrev_b32_e32 v242, 16, v167
	v_and_b32_e32 v243, 0xffff0000, v167
	v_pk_add_f32 v[236:237], v[236:237], v[232:233]
	v_pk_add_f32 v[238:239], v[238:239], v[234:235]
	v_pk_add_f32 v[240:241], v[240:241], v[98:99]
	v_pk_add_f32 v[242:243], v[242:243], v[100:101]
	v_pk_add_f32 v[236:237], v[236:237], 0 op_sel_hi:[1,0]
	v_pk_add_f32 v[238:239], v[238:239], 0 op_sel_hi:[1,0]
	v_pk_add_f32 v[240:241], v[240:241], 0 op_sel_hi:[1,0]
	v_pk_add_f32 v[242:243], v[242:243], 0 op_sel_hi:[1,0]
	s_nop 0
	v_cvt_pk_bf16_f32 v130, v236, v237
	v_cvt_pk_bf16_f32 v131, v238, v239
	v_cvt_pk_bf16_f32 v132, v240, v241
	v_cvt_pk_bf16_f32 v133, v242, v243
	global_store_dwordx2 v228, v[130:131], s[42:43] offset:64
	global_store_dwordx2 v229, v[132:133], s[42:43] offset:64
	s_add_u32 s42, s52, 0x10000
	s_addc_u32 s43, s53, 0
	s_waitcnt vmcnt(28)
	v_mov_b32_e32 v232, v94
	v_mov_b32_e32 v233, v95
	v_mov_b32_e32 v234, v96
	v_mov_b32_e32 v235, v97
	v_mov_b32_dpp v232, v90 row_ror:8 row_mask:0xf bank_mask:0xc
	v_mov_b32_dpp v90, v94 row_ror:8 row_mask:0xf bank_mask:0x3
	v_mov_b32_dpp v233, v91 row_ror:8 row_mask:0xf bank_mask:0xc
	v_mov_b32_dpp v91, v95 row_ror:8 row_mask:0xf bank_mask:0x3
	v_mov_b32_dpp v234, v92 row_ror:8 row_mask:0xf bank_mask:0xc
	v_mov_b32_dpp v92, v96 row_ror:8 row_mask:0xf bank_mask:0x3
	v_mov_b32_dpp v235, v93 row_ror:8 row_mask:0xf bank_mask:0xc
	v_mov_b32_dpp v93, v97 row_ror:8 row_mask:0xf bank_mask:0x3
	v_lshlrev_b32_e32 v236, 16, v168
	v_and_b32_e32 v237, 0xffff0000, v168
	v_lshlrev_b32_e32 v238, 16, v169
	v_and_b32_e32 v239, 0xffff0000, v169
	v_lshlrev_b32_e32 v240, 16, v172
	v_and_b32_e32 v241, 0xffff0000, v172
	v_lshlrev_b32_e32 v242, 16, v173
	v_and_b32_e32 v243, 0xffff0000, v173
	v_pk_add_f32 v[236:237], v[236:237], v[232:233]
	v_pk_add_f32 v[238:239], v[238:239], v[234:235]
	v_pk_add_f32 v[240:241], v[240:241], v[90:91]
	v_pk_add_f32 v[242:243], v[242:243], v[92:93]
	v_pk_add_f32 v[236:237], v[236:237], 0 op_sel_hi:[1,0]
	v_pk_add_f32 v[238:239], v[238:239], 0 op_sel_hi:[1,0]
	v_pk_add_f32 v[240:241], v[240:241], 0 op_sel_hi:[1,0]
	v_pk_add_f32 v[242:243], v[242:243], 0 op_sel_hi:[1,0]
	s_nop 0
	v_cvt_pk_bf16_f32 v244, v236, v237
	v_cvt_pk_bf16_f32 v245, v238, v239
	v_cvt_pk_bf16_f32 v246, v240, v241
	v_cvt_pk_bf16_f32 v247, v242, v243
	global_store_dwordx2 v228, v[244:245], s[42:43]
	global_store_dwordx2 v229, v[246:247], s[42:43]
	v_mov_b32_e32 v232, v86
	v_mov_b32_e32 v233, v87
	v_mov_b32_e32 v234, v88
	v_mov_b32_e32 v235, v89
	v_mov_b32_dpp v232, v82 row_ror:8 row_mask:0xf bank_mask:0xc
	v_mov_b32_dpp v82, v86 row_ror:8 row_mask:0xf bank_mask:0x3
	v_mov_b32_dpp v233, v83 row_ror:8 row_mask:0xf bank_mask:0xc
	v_mov_b32_dpp v83, v87 row_ror:8 row_mask:0xf bank_mask:0x3
	v_mov_b32_dpp v234, v84 row_ror:8 row_mask:0xf bank_mask:0xc
	v_mov_b32_dpp v84, v88 row_ror:8 row_mask:0xf bank_mask:0x3
	v_mov_b32_dpp v235, v85 row_ror:8 row_mask:0xf bank_mask:0xc
	v_mov_b32_dpp v85, v89 row_ror:8 row_mask:0xf bank_mask:0x3
	v_lshlrev_b32_e32 v236, 16, v170
	v_and_b32_e32 v237, 0xffff0000, v170
	v_lshlrev_b32_e32 v238, 16, v171
	v_and_b32_e32 v239, 0xffff0000, v171
	v_lshlrev_b32_e32 v240, 16, v174
	v_and_b32_e32 v241, 0xffff0000, v174
	v_lshlrev_b32_e32 v242, 16, v175
	v_and_b32_e32 v243, 0xffff0000, v175
	v_pk_add_f32 v[236:237], v[236:237], v[232:233]
	v_pk_add_f32 v[238:239], v[238:239], v[234:235]
	v_pk_add_f32 v[240:241], v[240:241], v[82:83]
	v_pk_add_f32 v[242:243], v[242:243], v[84:85]
	v_pk_add_f32 v[236:237], v[236:237], 0 op_sel_hi:[1,0]
	v_pk_add_f32 v[238:239], v[238:239], 0 op_sel_hi:[1,0]
	v_pk_add_f32 v[240:241], v[240:241], 0 op_sel_hi:[1,0]
	v_pk_add_f32 v[242:243], v[242:243], 0 op_sel_hi:[1,0]
	s_nop 0
	v_cvt_pk_bf16_f32 v130, v236, v237
	v_cvt_pk_bf16_f32 v131, v238, v239
	v_cvt_pk_bf16_f32 v132, v240, v241
	v_cvt_pk_bf16_f32 v133, v242, v243
	global_store_dwordx2 v228, v[130:131], s[42:43] offset:64
	global_store_dwordx2 v229, v[132:133], s[42:43] offset:64
	s_add_u32 s42, s52, 0x18000
	s_addc_u32 s43, s53, 0
	s_waitcnt vmcnt(28)
	v_mov_b32_e32 v232, v78
	v_mov_b32_e32 v233, v79
	v_mov_b32_e32 v234, v80
	v_mov_b32_e32 v235, v81
	v_mov_b32_dpp v232, v74 row_ror:8 row_mask:0xf bank_mask:0xc
	v_mov_b32_dpp v74, v78 row_ror:8 row_mask:0xf bank_mask:0x3
	v_mov_b32_dpp v233, v75 row_ror:8 row_mask:0xf bank_mask:0xc
	v_mov_b32_dpp v75, v79 row_ror:8 row_mask:0xf bank_mask:0x3
	v_mov_b32_dpp v234, v76 row_ror:8 row_mask:0xf bank_mask:0xc
	v_mov_b32_dpp v76, v80 row_ror:8 row_mask:0xf bank_mask:0x3
	v_mov_b32_dpp v235, v77 row_ror:8 row_mask:0xf bank_mask:0xc
	v_mov_b32_dpp v77, v81 row_ror:8 row_mask:0xf bank_mask:0x3
	v_lshlrev_b32_e32 v236, 16, v176
	v_and_b32_e32 v237, 0xffff0000, v176
	v_lshlrev_b32_e32 v238, 16, v177
	v_and_b32_e32 v239, 0xffff0000, v177
	v_lshlrev_b32_e32 v240, 16, v180
	v_and_b32_e32 v241, 0xffff0000, v180
	v_lshlrev_b32_e32 v242, 16, v181
	v_and_b32_e32 v243, 0xffff0000, v181
	v_pk_add_f32 v[236:237], v[236:237], v[232:233]
	v_pk_add_f32 v[238:239], v[238:239], v[234:235]
	v_pk_add_f32 v[240:241], v[240:241], v[74:75]
	v_pk_add_f32 v[242:243], v[242:243], v[76:77]
	v_pk_add_f32 v[236:237], v[236:237], 0 op_sel_hi:[1,0]
	v_pk_add_f32 v[238:239], v[238:239], 0 op_sel_hi:[1,0]
	v_pk_add_f32 v[240:241], v[240:241], 0 op_sel_hi:[1,0]
	v_pk_add_f32 v[242:243], v[242:243], 0 op_sel_hi:[1,0]
	s_nop 0
	v_cvt_pk_bf16_f32 v244, v236, v237
	v_cvt_pk_bf16_f32 v245, v238, v239
	v_cvt_pk_bf16_f32 v246, v240, v241
	v_cvt_pk_bf16_f32 v247, v242, v243
	global_store_dwordx2 v228, v[244:245], s[42:43]
	global_store_dwordx2 v229, v[246:247], s[42:43]
	v_mov_b32_e32 v232, v70
	v_mov_b32_e32 v233, v71
	v_mov_b32_e32 v234, v72
	v_mov_b32_e32 v235, v73
	v_mov_b32_dpp v232, v66 row_ror:8 row_mask:0xf bank_mask:0xc
	v_mov_b32_dpp v66, v70 row_ror:8 row_mask:0xf bank_mask:0x3
	v_mov_b32_dpp v233, v67 row_ror:8 row_mask:0xf bank_mask:0xc
	v_mov_b32_dpp v67, v71 row_ror:8 row_mask:0xf bank_mask:0x3
	v_mov_b32_dpp v234, v68 row_ror:8 row_mask:0xf bank_mask:0xc
	v_mov_b32_dpp v68, v72 row_ror:8 row_mask:0xf bank_mask:0x3
	v_mov_b32_dpp v235, v69 row_ror:8 row_mask:0xf bank_mask:0xc
	v_mov_b32_dpp v69, v73 row_ror:8 row_mask:0xf bank_mask:0x3
	v_lshlrev_b32_e32 v236, 16, v178
	v_and_b32_e32 v237, 0xffff0000, v178
	v_lshlrev_b32_e32 v238, 16, v179
	v_and_b32_e32 v239, 0xffff0000, v179
	v_lshlrev_b32_e32 v240, 16, v182
	v_and_b32_e32 v241, 0xffff0000, v182
	v_lshlrev_b32_e32 v242, 16, v183
	v_and_b32_e32 v243, 0xffff0000, v183
	v_pk_add_f32 v[236:237], v[236:237], v[232:233]
	v_pk_add_f32 v[238:239], v[238:239], v[234:235]
	v_pk_add_f32 v[240:241], v[240:241], v[66:67]
	v_pk_add_f32 v[242:243], v[242:243], v[68:69]
	v_pk_add_f32 v[236:237], v[236:237], 0 op_sel_hi:[1,0]
	v_pk_add_f32 v[238:239], v[238:239], 0 op_sel_hi:[1,0]
	v_pk_add_f32 v[240:241], v[240:241], 0 op_sel_hi:[1,0]
	v_pk_add_f32 v[242:243], v[242:243], 0 op_sel_hi:[1,0]
	s_nop 0
	v_cvt_pk_bf16_f32 v130, v236, v237
	v_cvt_pk_bf16_f32 v131, v238, v239
	v_cvt_pk_bf16_f32 v132, v240, v241
	v_cvt_pk_bf16_f32 v133, v242, v243
	global_store_dwordx2 v228, v[130:131], s[42:43] offset:64
	global_store_dwordx2 v229, v[132:133], s[42:43] offset:64
	s_add_u32 s42, s52, 0x40000
	s_addc_u32 s43, s53, 0
	s_waitcnt vmcnt(28)
	v_mov_b32_e32 v232, v62
	v_mov_b32_e32 v233, v63
	v_mov_b32_e32 v234, v64
	v_mov_b32_e32 v235, v65
	v_mov_b32_dpp v232, v58 row_ror:8 row_mask:0xf bank_mask:0xc
	v_mov_b32_dpp v58, v62 row_ror:8 row_mask:0xf bank_mask:0x3
	v_mov_b32_dpp v233, v59 row_ror:8 row_mask:0xf bank_mask:0xc
	v_mov_b32_dpp v59, v63 row_ror:8 row_mask:0xf bank_mask:0x3
	v_mov_b32_dpp v234, v60 row_ror:8 row_mask:0xf bank_mask:0xc
	v_mov_b32_dpp v60, v64 row_ror:8 row_mask:0xf bank_mask:0x3
	v_mov_b32_dpp v235, v61 row_ror:8 row_mask:0xf bank_mask:0xc
	v_mov_b32_dpp v61, v65 row_ror:8 row_mask:0xf bank_mask:0x3
	v_lshlrev_b32_e32 v236, 16, v184
	v_and_b32_e32 v237, 0xffff0000, v184
	v_lshlrev_b32_e32 v238, 16, v185
	v_and_b32_e32 v239, 0xffff0000, v185
	v_lshlrev_b32_e32 v240, 16, v188
	v_and_b32_e32 v241, 0xffff0000, v188
	v_lshlrev_b32_e32 v242, 16, v189
	v_and_b32_e32 v243, 0xffff0000, v189
	v_pk_add_f32 v[236:237], v[236:237], v[232:233]
	v_pk_add_f32 v[238:239], v[238:239], v[234:235]
	v_pk_add_f32 v[240:241], v[240:241], v[58:59]
	v_pk_add_f32 v[242:243], v[242:243], v[60:61]
	v_pk_add_f32 v[236:237], v[236:237], 0 op_sel_hi:[1,0]
	v_pk_add_f32 v[238:239], v[238:239], 0 op_sel_hi:[1,0]
	v_pk_add_f32 v[240:241], v[240:241], 0 op_sel_hi:[1,0]
	v_pk_add_f32 v[242:243], v[242:243], 0 op_sel_hi:[1,0]
	s_nop 0
	v_cvt_pk_bf16_f32 v244, v236, v237
	v_cvt_pk_bf16_f32 v245, v238, v239
	v_cvt_pk_bf16_f32 v246, v240, v241
	v_cvt_pk_bf16_f32 v247, v242, v243
	global_store_dwordx2 v228, v[244:245], s[42:43]
	global_store_dwordx2 v229, v[246:247], s[42:43]
	v_mov_b32_e32 v232, v54
	v_mov_b32_e32 v233, v55
	v_mov_b32_e32 v234, v56
	v_mov_b32_e32 v235, v57
	v_mov_b32_dpp v232, v50 row_ror:8 row_mask:0xf bank_mask:0xc
	v_mov_b32_dpp v50, v54 row_ror:8 row_mask:0xf bank_mask:0x3
	v_mov_b32_dpp v233, v51 row_ror:8 row_mask:0xf bank_mask:0xc
	v_mov_b32_dpp v51, v55 row_ror:8 row_mask:0xf bank_mask:0x3
	v_mov_b32_dpp v234, v52 row_ror:8 row_mask:0xf bank_mask:0xc
	v_mov_b32_dpp v52, v56 row_ror:8 row_mask:0xf bank_mask:0x3
	v_mov_b32_dpp v235, v53 row_ror:8 row_mask:0xf bank_mask:0xc
	v_mov_b32_dpp v53, v57 row_ror:8 row_mask:0xf bank_mask:0x3
	v_lshlrev_b32_e32 v236, 16, v186
	v_and_b32_e32 v237, 0xffff0000, v186
	v_lshlrev_b32_e32 v238, 16, v187
	v_and_b32_e32 v239, 0xffff0000, v187
	v_lshlrev_b32_e32 v240, 16, v190
	v_and_b32_e32 v241, 0xffff0000, v190
	v_lshlrev_b32_e32 v242, 16, v191
	v_and_b32_e32 v243, 0xffff0000, v191
	v_pk_add_f32 v[236:237], v[236:237], v[232:233]
	v_pk_add_f32 v[238:239], v[238:239], v[234:235]
	v_pk_add_f32 v[240:241], v[240:241], v[50:51]
	v_pk_add_f32 v[242:243], v[242:243], v[52:53]
	v_pk_add_f32 v[236:237], v[236:237], 0 op_sel_hi:[1,0]
	v_pk_add_f32 v[238:239], v[238:239], 0 op_sel_hi:[1,0]
	v_pk_add_f32 v[240:241], v[240:241], 0 op_sel_hi:[1,0]
	v_pk_add_f32 v[242:243], v[242:243], 0 op_sel_hi:[1,0]
	s_nop 0
	v_cvt_pk_bf16_f32 v130, v236, v237
	v_cvt_pk_bf16_f32 v131, v238, v239
	v_cvt_pk_bf16_f32 v132, v240, v241
	v_cvt_pk_bf16_f32 v133, v242, v243
	global_store_dwordx2 v228, v[130:131], s[42:43] offset:64
	global_store_dwordx2 v229, v[132:133], s[42:43] offset:64
	s_add_u32 s42, s52, 0x48000
	s_addc_u32 s43, s53, 0
	s_waitcnt vmcnt(28)
	v_mov_b32_e32 v232, v46
	v_mov_b32_e32 v233, v47
	v_mov_b32_e32 v234, v48
	v_mov_b32_e32 v235, v49
	v_mov_b32_dpp v232, v42 row_ror:8 row_mask:0xf bank_mask:0xc
	v_mov_b32_dpp v42, v46 row_ror:8 row_mask:0xf bank_mask:0x3
	v_mov_b32_dpp v233, v43 row_ror:8 row_mask:0xf bank_mask:0xc
	v_mov_b32_dpp v43, v47 row_ror:8 row_mask:0xf bank_mask:0x3
	v_mov_b32_dpp v234, v44 row_ror:8 row_mask:0xf bank_mask:0xc
	v_mov_b32_dpp v44, v48 row_ror:8 row_mask:0xf bank_mask:0x3
	v_mov_b32_dpp v235, v45 row_ror:8 row_mask:0xf bank_mask:0xc
	v_mov_b32_dpp v45, v49 row_ror:8 row_mask:0xf bank_mask:0x3
	v_lshlrev_b32_e32 v236, 16, v192
	v_and_b32_e32 v237, 0xffff0000, v192
	v_lshlrev_b32_e32 v238, 16, v193
	v_and_b32_e32 v239, 0xffff0000, v193
	v_lshlrev_b32_e32 v240, 16, v196
	v_and_b32_e32 v241, 0xffff0000, v196
	v_lshlrev_b32_e32 v242, 16, v197
	v_and_b32_e32 v243, 0xffff0000, v197
	v_pk_add_f32 v[236:237], v[236:237], v[232:233]
	v_pk_add_f32 v[238:239], v[238:239], v[234:235]
	v_pk_add_f32 v[240:241], v[240:241], v[42:43]
	v_pk_add_f32 v[242:243], v[242:243], v[44:45]
	v_pk_add_f32 v[236:237], v[236:237], 0 op_sel_hi:[1,0]
	v_pk_add_f32 v[238:239], v[238:239], 0 op_sel_hi:[1,0]
	v_pk_add_f32 v[240:241], v[240:241], 0 op_sel_hi:[1,0]
	v_pk_add_f32 v[242:243], v[242:243], 0 op_sel_hi:[1,0]
	s_nop 0
	v_cvt_pk_bf16_f32 v244, v236, v237
	v_cvt_pk_bf16_f32 v245, v238, v239
	v_cvt_pk_bf16_f32 v246, v240, v241
	v_cvt_pk_bf16_f32 v247, v242, v243
	global_store_dwordx2 v228, v[244:245], s[42:43]
	global_store_dwordx2 v229, v[246:247], s[42:43]
	v_mov_b32_e32 v232, v38
	v_mov_b32_e32 v233, v39
	v_mov_b32_e32 v234, v40
	v_mov_b32_e32 v235, v41
	v_mov_b32_dpp v232, v34 row_ror:8 row_mask:0xf bank_mask:0xc
	v_mov_b32_dpp v34, v38 row_ror:8 row_mask:0xf bank_mask:0x3
	v_mov_b32_dpp v233, v35 row_ror:8 row_mask:0xf bank_mask:0xc
	v_mov_b32_dpp v35, v39 row_ror:8 row_mask:0xf bank_mask:0x3
	v_mov_b32_dpp v234, v36 row_ror:8 row_mask:0xf bank_mask:0xc
	v_mov_b32_dpp v36, v40 row_ror:8 row_mask:0xf bank_mask:0x3
	v_mov_b32_dpp v235, v37 row_ror:8 row_mask:0xf bank_mask:0xc
	v_mov_b32_dpp v37, v41 row_ror:8 row_mask:0xf bank_mask:0x3
	v_lshlrev_b32_e32 v236, 16, v194
	v_and_b32_e32 v237, 0xffff0000, v194
	v_lshlrev_b32_e32 v238, 16, v195
	v_and_b32_e32 v239, 0xffff0000, v195
	v_lshlrev_b32_e32 v240, 16, v198
	v_and_b32_e32 v241, 0xffff0000, v198
	v_lshlrev_b32_e32 v242, 16, v199
	v_and_b32_e32 v243, 0xffff0000, v199
	v_pk_add_f32 v[236:237], v[236:237], v[232:233]
	v_pk_add_f32 v[238:239], v[238:239], v[234:235]
	v_pk_add_f32 v[240:241], v[240:241], v[34:35]
	v_pk_add_f32 v[242:243], v[242:243], v[36:37]
	v_pk_add_f32 v[236:237], v[236:237], 0 op_sel_hi:[1,0]
	v_pk_add_f32 v[238:239], v[238:239], 0 op_sel_hi:[1,0]
	v_pk_add_f32 v[240:241], v[240:241], 0 op_sel_hi:[1,0]
	v_pk_add_f32 v[242:243], v[242:243], 0 op_sel_hi:[1,0]
	s_nop 0
	v_cvt_pk_bf16_f32 v130, v236, v237
	v_cvt_pk_bf16_f32 v131, v238, v239
	v_cvt_pk_bf16_f32 v132, v240, v241
	v_cvt_pk_bf16_f32 v133, v242, v243
	global_store_dwordx2 v228, v[130:131], s[42:43] offset:64
	global_store_dwordx2 v229, v[132:133], s[42:43] offset:64
	s_add_u32 s42, s52, 0x50000
	s_addc_u32 s43, s53, 0
	s_waitcnt vmcnt(28)
	v_mov_b32_e32 v232, v30
	v_mov_b32_e32 v233, v31
	v_mov_b32_e32 v234, v32
	v_mov_b32_e32 v235, v33
	v_mov_b32_dpp v232, v26 row_ror:8 row_mask:0xf bank_mask:0xc
	v_mov_b32_dpp v26, v30 row_ror:8 row_mask:0xf bank_mask:0x3
	v_mov_b32_dpp v233, v27 row_ror:8 row_mask:0xf bank_mask:0xc
	v_mov_b32_dpp v27, v31 row_ror:8 row_mask:0xf bank_mask:0x3
	v_mov_b32_dpp v234, v28 row_ror:8 row_mask:0xf bank_mask:0xc
	v_mov_b32_dpp v28, v32 row_ror:8 row_mask:0xf bank_mask:0x3
	v_mov_b32_dpp v235, v29 row_ror:8 row_mask:0xf bank_mask:0xc
	v_mov_b32_dpp v29, v33 row_ror:8 row_mask:0xf bank_mask:0x3
	v_lshlrev_b32_e32 v236, 16, v208
	v_and_b32_e32 v237, 0xffff0000, v208
	v_lshlrev_b32_e32 v238, 16, v209
	v_and_b32_e32 v239, 0xffff0000, v209
	v_lshlrev_b32_e32 v240, 16, v212
	v_and_b32_e32 v241, 0xffff0000, v212
	v_lshlrev_b32_e32 v242, 16, v213
	v_and_b32_e32 v243, 0xffff0000, v213
	v_pk_add_f32 v[236:237], v[236:237], v[232:233]
	v_pk_add_f32 v[238:239], v[238:239], v[234:235]
	v_pk_add_f32 v[240:241], v[240:241], v[26:27]
	v_pk_add_f32 v[242:243], v[242:243], v[28:29]
	v_pk_add_f32 v[236:237], v[236:237], 0 op_sel_hi:[1,0]
	v_pk_add_f32 v[238:239], v[238:239], 0 op_sel_hi:[1,0]
	v_pk_add_f32 v[240:241], v[240:241], 0 op_sel_hi:[1,0]
	v_pk_add_f32 v[242:243], v[242:243], 0 op_sel_hi:[1,0]
	s_nop 0
	v_cvt_pk_bf16_f32 v244, v236, v237
	v_cvt_pk_bf16_f32 v245, v238, v239
	v_cvt_pk_bf16_f32 v246, v240, v241
	v_cvt_pk_bf16_f32 v247, v242, v243
	global_store_dwordx2 v228, v[244:245], s[42:43]
	global_store_dwordx2 v229, v[246:247], s[42:43]
	v_mov_b32_e32 v232, v22
	v_mov_b32_e32 v233, v23
	v_mov_b32_e32 v234, v24
	v_mov_b32_e32 v235, v25
	v_mov_b32_dpp v232, v18 row_ror:8 row_mask:0xf bank_mask:0xc
	v_mov_b32_dpp v18, v22 row_ror:8 row_mask:0xf bank_mask:0x3
	v_mov_b32_dpp v233, v19 row_ror:8 row_mask:0xf bank_mask:0xc
	v_mov_b32_dpp v19, v23 row_ror:8 row_mask:0xf bank_mask:0x3
	v_mov_b32_dpp v234, v20 row_ror:8 row_mask:0xf bank_mask:0xc
	v_mov_b32_dpp v20, v24 row_ror:8 row_mask:0xf bank_mask:0x3
	v_mov_b32_dpp v235, v21 row_ror:8 row_mask:0xf bank_mask:0xc
	v_mov_b32_dpp v21, v25 row_ror:8 row_mask:0xf bank_mask:0x3
	v_lshlrev_b32_e32 v236, 16, v210
	v_and_b32_e32 v237, 0xffff0000, v210
	v_lshlrev_b32_e32 v238, 16, v211
	v_and_b32_e32 v239, 0xffff0000, v211
	v_lshlrev_b32_e32 v240, 16, v214
	v_and_b32_e32 v241, 0xffff0000, v214
	v_lshlrev_b32_e32 v242, 16, v215
	v_and_b32_e32 v243, 0xffff0000, v215
	v_pk_add_f32 v[236:237], v[236:237], v[232:233]
	v_pk_add_f32 v[238:239], v[238:239], v[234:235]
	v_pk_add_f32 v[240:241], v[240:241], v[18:19]
	v_pk_add_f32 v[242:243], v[242:243], v[20:21]
	v_pk_add_f32 v[236:237], v[236:237], 0 op_sel_hi:[1,0]
	v_pk_add_f32 v[238:239], v[238:239], 0 op_sel_hi:[1,0]
	v_pk_add_f32 v[240:241], v[240:241], 0 op_sel_hi:[1,0]
	v_pk_add_f32 v[242:243], v[242:243], 0 op_sel_hi:[1,0]
	s_nop 0
	v_cvt_pk_bf16_f32 v130, v236, v237
	v_cvt_pk_bf16_f32 v131, v238, v239
	v_cvt_pk_bf16_f32 v132, v240, v241
	v_cvt_pk_bf16_f32 v133, v242, v243
	global_store_dwordx2 v228, v[130:131], s[42:43] offset:64
	global_store_dwordx2 v229, v[132:133], s[42:43] offset:64
	s_add_u32 s42, s52, 0x58000
	s_addc_u32 s43, s53, 0
	s_waitcnt vmcnt(28)
	v_mov_b32_e32 v232, v14
	v_mov_b32_e32 v233, v15
	v_mov_b32_e32 v234, v16
	v_mov_b32_e32 v235, v17
	v_mov_b32_dpp v232, v10 row_ror:8 row_mask:0xf bank_mask:0xc
	v_mov_b32_dpp v10, v14 row_ror:8 row_mask:0xf bank_mask:0x3
	v_mov_b32_dpp v233, v11 row_ror:8 row_mask:0xf bank_mask:0xc
	v_mov_b32_dpp v11, v15 row_ror:8 row_mask:0xf bank_mask:0x3
	v_mov_b32_dpp v234, v12 row_ror:8 row_mask:0xf bank_mask:0xc
	v_mov_b32_dpp v12, v16 row_ror:8 row_mask:0xf bank_mask:0x3
	v_mov_b32_dpp v235, v13 row_ror:8 row_mask:0xf bank_mask:0xc
	v_mov_b32_dpp v13, v17 row_ror:8 row_mask:0xf bank_mask:0x3
	v_lshlrev_b32_e32 v236, 16, v216
	v_and_b32_e32 v237, 0xffff0000, v216
	v_lshlrev_b32_e32 v238, 16, v217
	v_and_b32_e32 v239, 0xffff0000, v217
	v_lshlrev_b32_e32 v240, 16, v220
	v_and_b32_e32 v241, 0xffff0000, v220
	v_lshlrev_b32_e32 v242, 16, v221
	v_and_b32_e32 v243, 0xffff0000, v221
	v_pk_add_f32 v[236:237], v[236:237], v[232:233]
	v_pk_add_f32 v[238:239], v[238:239], v[234:235]
	v_pk_add_f32 v[240:241], v[240:241], v[10:11]
	v_pk_add_f32 v[242:243], v[242:243], v[12:13]
	v_pk_add_f32 v[236:237], v[236:237], 0 op_sel_hi:[1,0]
	v_pk_add_f32 v[238:239], v[238:239], 0 op_sel_hi:[1,0]
	v_pk_add_f32 v[240:241], v[240:241], 0 op_sel_hi:[1,0]
	v_pk_add_f32 v[242:243], v[242:243], 0 op_sel_hi:[1,0]
	s_nop 0
	v_cvt_pk_bf16_f32 v244, v236, v237
	v_cvt_pk_bf16_f32 v245, v238, v239
	v_cvt_pk_bf16_f32 v246, v240, v241
	v_cvt_pk_bf16_f32 v247, v242, v243
	global_store_dwordx2 v228, v[244:245], s[42:43]
	global_store_dwordx2 v229, v[246:247], s[42:43]
	v_mov_b32_e32 v232, v6
	v_mov_b32_e32 v233, v7
	v_mov_b32_e32 v234, v8
	v_mov_b32_e32 v235, v9
	v_mov_b32_dpp v232, v2 row_ror:8 row_mask:0xf bank_mask:0xc
	v_mov_b32_dpp v2, v6 row_ror:8 row_mask:0xf bank_mask:0x3
	v_mov_b32_dpp v233, v3 row_ror:8 row_mask:0xf bank_mask:0xc
	v_mov_b32_dpp v3, v7 row_ror:8 row_mask:0xf bank_mask:0x3
	v_mov_b32_dpp v234, v4 row_ror:8 row_mask:0xf bank_mask:0xc
	v_mov_b32_dpp v4, v8 row_ror:8 row_mask:0xf bank_mask:0x3
	v_mov_b32_dpp v235, v5 row_ror:8 row_mask:0xf bank_mask:0xc
	v_mov_b32_dpp v5, v9 row_ror:8 row_mask:0xf bank_mask:0x3
	v_lshlrev_b32_e32 v236, 16, v218
	v_and_b32_e32 v237, 0xffff0000, v218
	v_lshlrev_b32_e32 v238, 16, v219
	v_and_b32_e32 v239, 0xffff0000, v219
	v_lshlrev_b32_e32 v240, 16, v222
	v_and_b32_e32 v241, 0xffff0000, v222
	v_lshlrev_b32_e32 v242, 16, v223
	v_and_b32_e32 v243, 0xffff0000, v223
	v_pk_add_f32 v[236:237], v[236:237], v[232:233]
	v_pk_add_f32 v[238:239], v[238:239], v[234:235]
	v_pk_add_f32 v[240:241], v[240:241], v[2:3]
	v_pk_add_f32 v[242:243], v[242:243], v[4:5]
	v_pk_add_f32 v[236:237], v[236:237], 0 op_sel_hi:[1,0]
	v_pk_add_f32 v[238:239], v[238:239], 0 op_sel_hi:[1,0]
	v_pk_add_f32 v[240:241], v[240:241], 0 op_sel_hi:[1,0]
	v_pk_add_f32 v[242:243], v[242:243], 0 op_sel_hi:[1,0]
	s_nop 0
	v_cvt_pk_bf16_f32 v130, v236, v237
	v_cvt_pk_bf16_f32 v131, v238, v239
	v_cvt_pk_bf16_f32 v132, v240, v241
	v_cvt_pk_bf16_f32 v133, v242, v243
	global_store_dwordx2 v228, v[130:131], s[42:43] offset:64
	global_store_dwordx2 v229, v[132:133], s[42:43] offset:64
	s_branch .Lrs_a_end
	v_add_co_u32_e32 v126, vcc, 0x4000, v140
	global_load_dwordx2 v[128:129], v[140:141], off nt
	s_nop 0
	v_addc_co_u32_e32 v127, vcc, 0, v141, vcc
	global_load_dwordx2 v[132:133], v[126:127], off nt
	s_waitcnt vmcnt(0)
	v_lshlrev_b32_e32 v126, 16, v128
	v_and_b32_e32 v127, 0xffff0000, v128
	v_lshlrev_b32_e32 v128, 16, v129
	v_and_b32_e32 v129, 0xffff0000, v129
	v_lshlrev_b32_e32 v130, 16, v132
	v_and_b32_e32 v131, 0xffff0000, v132
	v_lshlrev_b32_e32 v132, 16, v133
	v_and_b32_e32 v133, 0xffff0000, v133
	v_lshl_add_u64 v[138:139], v[142:143], 2, s[48:49]
	s_cbranch_execnz .LBB0_435

.Lrs_a_end:
	s_andn2_b64 vcc, exec, s[40:41]
	s_mov_b64 s[0:1], -1
	s_cbranch_vccnz .LBB0_421
	s_andn2_b64 vcc, exec, s[50:51]
	s_cbranch_vccnz .LBB0_420
	s_barrier
	s_branch .LBB0_420
